# v83: v76 + non-temporal hint on the deferred weight conversion's loads and stores (beside gdn_gb)
# baseline (speedup 1.0000x reference)
.LBB0_1682:
	s_lshl_b32 s8, s13, 6
	s_ashr_i32 s13, s12, 31
	s_lshl_b64 s[12:13], s[12:13], 2
	s_add_u32 s12, s0, s12
	s_waitcnt vmcnt(0)
	v_or_b32_e32 v96, s8, v106
	s_addc_u32 s13, s1, s13
	v_lshlrev_b32_e32 v2, 2, v0
	v_lshl_add_u64 v[92:93], s[12:13], 0, v[2:3]
	v_or_b32_e32 v2, 8, v96
	v_mad_u64_u32 v[70:71], s[12:13], v2, s22, 0
	v_or_b32_e32 v2, 16, v96
	v_mad_u64_u32 v[76:77], s[12:13], v2, s22, 0
	v_or_b32_e32 v2, 24, v96
	v_mad_u64_u32 v[78:79], s[12:13], v2, s22, 0
	v_or_b32_e32 v2, 32, v96
	v_mad_u64_u32 v[84:85], s[12:13], v2, s22, 0
	v_or_b32_e32 v2, 40, v96
	v_mad_u64_u32 v[86:87], s[12:13], v2, s22, 0
	v_or_b32_e32 v2, 48, v96
	s_ashr_i32 s9, s8, 31
	v_mad_u64_u32 v[94:95], s[12:13], v2, s22, 0
	v_or_b32_e32 v2, 56, v96
	s_mul_i32 s9, s9, s22
	v_mad_u64_u32 v[68:69], s[12:13], v96, s22, 0
	v_mad_u64_u32 v[96:97], s[12:13], v2, s22, 0
	v_add_u32_e32 v69, s9, v69
	v_add_u32_e32 v71, s9, v71
	v_add_u32_e32 v77, s9, v77
	v_add_u32_e32 v79, s9, v79
	v_add_u32_e32 v85, s9, v85
	v_add_u32_e32 v87, s9, v87
	v_add_u32_e32 v95, s9, v95
	v_add_u32_e32 v97, s9, v97
	v_lshl_add_u64 v[68:69], v[68:69], 2, v[92:93]
	v_lshl_add_u64 v[72:73], v[70:71], 2, v[92:93]
	v_lshl_add_u64 v[76:77], v[76:77], 2, v[92:93]
	v_lshl_add_u64 v[80:81], v[78:79], 2, v[92:93]
	v_lshl_add_u64 v[84:85], v[84:85], 2, v[92:93]
	v_lshl_add_u64 v[88:89], v[86:87], 2, v[92:93]
	v_lshl_add_u64 v[94:95], v[94:95], 2, v[92:93]
	v_lshl_add_u64 v[96:97], v[96:97], 2, v[92:93]
	global_load_dwordx4 v[68:71], v[68:69], off nt
	s_nop 0
	global_load_dwordx4 v[72:75], v[72:73], off nt
	s_nop 0
	global_load_dwordx4 v[76:79], v[76:77], off nt
	s_nop 0
	global_load_dwordx4 v[80:83], v[80:81], off nt
	s_nop 0
	global_load_dwordx4 v[84:87], v[84:85], off nt
	s_nop 0
	global_load_dwordx4 v[88:91], v[88:89], off nt
	s_nop 0
	global_load_dwordx4 v[92:95], v[94:95], off nt
	s_nop 0
	global_load_dwordx4 v[96:99], v[96:97], off nt

.LBB0_1689:
	s_ashr_i32 s13, s12, 31
	s_lshl_b32 s14, s9, 6
	s_lshl_b64 s[12:13], s[12:13], 2
	s_add_u32 s12, s0, s12
	s_waitcnt vmcnt(1)
	v_or_b32_e32 v64, s14, v106
	s_addc_u32 s13, s1, s13
	v_lshlrev_b32_e32 v2, 2, v0
	s_waitcnt vmcnt(0)
	v_lshl_add_u64 v[56:57], s[12:13], 0, v[2:3]
	v_or_b32_e32 v2, 8, v64
	v_mad_u64_u32 v[38:39], s[12:13], v2, s22, 0
	v_or_b32_e32 v2, 16, v64
	v_mad_u64_u32 v[44:45], s[12:13], v2, s22, 0
	v_or_b32_e32 v2, 24, v64
	v_mad_u64_u32 v[46:47], s[12:13], v2, s22, 0
	v_or_b32_e32 v2, 32, v64
	v_mad_u64_u32 v[52:53], s[12:13], v2, s22, 0
	v_or_b32_e32 v2, 40, v64
	v_mad_u64_u32 v[54:55], s[12:13], v2, s22, 0
	v_or_b32_e32 v2, 48, v64
	s_ashr_i32 s9, s14, 31
	v_mad_u64_u32 v[58:59], s[12:13], v2, s22, 0
	v_or_b32_e32 v2, 56, v64
	s_mul_i32 s9, s9, s22
	v_mad_u64_u32 v[36:37], s[12:13], v64, s22, 0
	v_mad_u64_u32 v[64:65], s[12:13], v2, s22, 0
	v_add_u32_e32 v37, s9, v37
	v_add_u32_e32 v39, s9, v39
	v_add_u32_e32 v45, s9, v45
	v_add_u32_e32 v47, s9, v47
	v_add_u32_e32 v53, s9, v53
	v_add_u32_e32 v55, s9, v55
	v_add_u32_e32 v59, s9, v59
	v_add_u32_e32 v65, s9, v65
	v_lshl_add_u64 v[36:37], v[36:37], 2, v[56:57]
	v_lshl_add_u64 v[38:39], v[38:39], 2, v[56:57]
	v_lshl_add_u64 v[44:45], v[44:45], 2, v[56:57]
	v_lshl_add_u64 v[46:47], v[46:47], 2, v[56:57]
	v_lshl_add_u64 v[52:53], v[52:53], 2, v[56:57]
	v_lshl_add_u64 v[54:55], v[54:55], 2, v[56:57]
	v_lshl_add_u64 v[58:59], v[58:59], 2, v[56:57]
	v_lshl_add_u64 v[56:57], v[64:65], 2, v[56:57]
	global_load_dwordx4 v[40:43], v[36:37], off nt
	s_nop 0
	global_load_dwordx4 v[36:39], v[38:39], off nt
	s_nop 0
	global_load_dwordx4 v[48:51], v[44:45], off nt
	s_nop 0
	global_load_dwordx4 v[44:47], v[46:47], off nt
	s_nop 0
	global_load_dwordx4 v[60:63], v[52:53], off nt
	s_nop 0
	global_load_dwordx4 v[52:55], v[54:55], off nt
	s_nop 0
	global_load_dwordx4 v[64:67], v[58:59], off nt
	s_nop 0
	global_load_dwordx4 v[56:59], v[56:57], off nt

.LBB0_1698:
	s_lshl_b32 s14, s1, 6
	s_ashr_i32 s1, s0, 31
	v_or_b32_e32 v2, s14, v106
	v_lshl_add_u64 v[28:29], s[0:1], 2, v[102:103]
	s_ashr_i32 s0, s14, 31
	s_mul_i32 s2, s0, s22
	v_mad_u64_u32 v[4:5], s[0:1], v2, s22, 0
	v_or_b32_e32 v6, 8, v2
	v_or_b32_e32 v12, 16, v2
	v_or_b32_e32 v14, 24, v2
	v_or_b32_e32 v20, 32, v2
	v_or_b32_e32 v22, 40, v2
	v_or_b32_e32 v30, 48, v2
	v_or_b32_e32 v2, 56, v2
	v_mad_u64_u32 v[6:7], s[0:1], v6, s22, 0
	v_mad_u64_u32 v[12:13], s[0:1], v12, s22, 0
	v_mad_u64_u32 v[14:15], s[0:1], v14, s22, 0
	v_mad_u64_u32 v[20:21], s[0:1], v20, s22, 0
	v_mad_u64_u32 v[22:23], s[0:1], v22, s22, 0
	v_mad_u64_u32 v[30:31], s[0:1], v30, s22, 0
	v_mad_u64_u32 v[32:33], s[0:1], v2, s22, 0
	v_add_u32_e32 v5, s2, v5
	v_add_u32_e32 v7, s2, v7
	v_add_u32_e32 v13, s2, v13
	v_add_u32_e32 v15, s2, v15
	v_add_u32_e32 v21, s2, v21
	v_add_u32_e32 v23, s2, v23
	v_add_u32_e32 v31, s2, v31
	v_add_u32_e32 v33, s2, v33
	v_lshl_add_u64 v[4:5], v[4:5], 2, v[28:29]
	v_lshl_add_u64 v[6:7], v[6:7], 2, v[28:29]
	v_lshl_add_u64 v[12:13], v[12:13], 2, v[28:29]
	v_lshl_add_u64 v[14:15], v[14:15], 2, v[28:29]
	v_lshl_add_u64 v[20:21], v[20:21], 2, v[28:29]
	v_lshl_add_u64 v[22:23], v[22:23], 2, v[28:29]
	v_lshl_add_u64 v[30:31], v[30:31], 2, v[28:29]
	v_lshl_add_u64 v[28:29], v[32:33], 2, v[28:29]
	global_load_dwordx4 v[8:11], v[4:5], off nt
	s_nop 0
	global_load_dwordx4 v[4:7], v[6:7], off nt
	s_nop 0
	global_load_dwordx4 v[16:19], v[12:13], off nt
	s_nop 0
	global_load_dwordx4 v[12:15], v[14:15], off nt
	s_nop 0
	global_load_dwordx4 v[24:27], v[20:21], off nt
	s_nop 0
	global_load_dwordx4 v[20:23], v[22:23], off nt
	s_nop 0
	global_load_dwordx4 v[32:35], v[30:31], off nt
	s_nop 0
	global_load_dwordx4 v[28:31], v[28:29], off nt
.LBB0_1699:
	v_add_u32_e32 v2, 0x8000, v111
	s_waitcnt vmcnt(7)
	ds_write2_b32 v2, v68, v69 offset1:1
	v_add_u32_e32 v2, 0x8008, v111
	ds_write2_b32 v2, v70, v71 offset1:1
	v_add_u32_e32 v2, 0x8420, v111
	s_waitcnt vmcnt(6)
	ds_write2_b32 v2, v72, v73 offset1:1
	v_add_u32_e32 v2, 0x8428, v111
	ds_write2_b32 v2, v74, v75 offset1:1
	v_add_u32_e32 v2, 0x8840, v111
	s_waitcnt vmcnt(5)
	ds_write2_b32 v2, v76, v77 offset1:1
	v_add_u32_e32 v2, 0x8848, v111
	ds_write2_b32 v2, v78, v79 offset1:1
	v_add_u32_e32 v2, 0x8c60, v111
	s_waitcnt vmcnt(4)
	ds_write2_b32 v2, v80, v81 offset1:1
	v_add_u32_e32 v2, 0x8c68, v111
	ds_write2_b32 v2, v82, v83 offset1:1
	v_add_u32_e32 v2, 0x9080, v111
	s_waitcnt vmcnt(3)
	ds_write2_b32 v2, v84, v85 offset1:1
	v_add_u32_e32 v2, 0x9088, v111
	ds_write2_b32 v2, v86, v87 offset1:1
	v_add_u32_e32 v2, 0x94a0, v111
	s_waitcnt vmcnt(2)
	ds_write2_b32 v2, v88, v89 offset1:1
	v_add_u32_e32 v2, 0x94a8, v111
	ds_write2_b32 v2, v90, v91 offset1:1
	v_add_u32_e32 v2, 0x98c0, v111
	s_waitcnt vmcnt(1)
	ds_write2_b32 v2, v92, v93 offset1:1
	v_add_u32_e32 v2, 0x98c8, v111
	ds_write2_b32 v2, v94, v95 offset1:1
	v_add_u32_e32 v2, 0x9ce0, v111
	s_waitcnt vmcnt(0)
	ds_write2_b32 v2, v96, v97 offset1:1
	v_add_u32_e32 v2, 0x9ce8, v111
	ds_write2_b32 v2, v98, v99 offset1:1
	s_waitcnt lgkmcnt(0)
	v_add_u32_e32 v94, 0x8000, v110
	ds_read2_b32 v[72:73], v94 offset0:33 offset1:41
	ds_read2_b32 v[74:75], v94 offset1:8
	ds_read2_b32 v[76:77], v94 offset0:66 offset1:74
	ds_read2_b32 v[78:79], v94 offset0:99 offset1:107
	ds_read2_b32 v[80:81], v94 offset0:132 offset1:140
	ds_read2_b32 v[82:83], v94 offset0:165 offset1:173
	ds_read2_b32 v[84:85], v94 offset0:198 offset1:206
	ds_read2_b32 v[86:87], v94 offset0:231 offset1:239
	v_add_u32_e32 v2, s35, v106
	v_mad_u64_u32 v[90:91], s[0:1], v2, s25, 0
	s_waitcnt lgkmcnt(6)
	v_cvt_pk_bf16_f32 v68, v74, v72
	v_ashrrev_i32_e32 v72, 31, v2
	v_mov_b32_e32 v2, v91
	s_ashr_i32 s9, s8, 31
	v_mad_u64_u32 v[92:93], s[0:1], v72, s25, v[2:3]
	v_lshl_add_u64 v[88:89], s[8:9], 1, v[104:105]
	v_mov_b32_e32 v91, v92
	s_waitcnt lgkmcnt(4)
	v_cvt_pk_bf16_f32 v69, v76, v78
	s_waitcnt lgkmcnt(2)
	v_cvt_pk_bf16_f32 v70, v80, v82
	s_waitcnt lgkmcnt(0)
	v_cvt_pk_bf16_f32 v71, v84, v86
	v_lshl_add_u64 v[90:91], v[90:91], 1, v[88:89]
	v_add_u32_e32 v2, s35, v107
	global_store_dwordx4 v[90:91], v[68:71], off nt
	v_ashrrev_i32_e32 v74, 31, v2
	s_add_i32 s31, s31, s88
	v_cvt_pk_bf16_f32 v68, v75, v73
	v_mad_u64_u32 v[72:73], s[0:1], v2, s25, 0
	v_mov_b32_e32 v2, v73
	v_mad_u64_u32 v[74:75], s[0:1], v74, s25, v[2:3]
	v_mov_b32_e32 v73, v74
	v_cvt_pk_bf16_f32 v69, v77, v79
	v_cvt_pk_bf16_f32 v70, v81, v83
	v_cvt_pk_bf16_f32 v71, v85, v87
	v_lshl_add_u64 v[72:73], v[72:73], 1, v[88:89]
	ds_read2_b32 v[74:75], v94 offset0:16 offset1:24
	ds_read2_b32 v[76:77], v94 offset0:49 offset1:57
	ds_read2_b32 v[78:79], v94 offset0:82 offset1:90
	ds_read2_b32 v[80:81], v94 offset0:115 offset1:123
	ds_read2_b32 v[82:83], v94 offset0:148 offset1:156
	ds_read2_b32 v[84:85], v94 offset0:181 offset1:189
	ds_read2_b32 v[86:87], v94 offset0:214 offset1:222
	ds_read2_b32 v[90:91], v94 offset0:247 offset1:255
	v_add_u32_e32 v2, s35, v108
	global_store_dwordx4 v[72:73], v[68:71], off nt
	v_mad_u64_u32 v[72:73], s[0:1], v2, s25, 0
	s_waitcnt lgkmcnt(6)
	v_cvt_pk_bf16_f32 v68, v74, v76
	v_ashrrev_i32_e32 v74, 31, v2
	v_mov_b32_e32 v2, v73
	v_mad_u64_u32 v[92:93], s[0:1], v74, s25, v[2:3]
	v_mov_b32_e32 v73, v92
	s_waitcnt lgkmcnt(4)
	v_cvt_pk_bf16_f32 v69, v78, v80
	s_waitcnt lgkmcnt(2)
	v_cvt_pk_bf16_f32 v70, v82, v84
	s_waitcnt lgkmcnt(0)
	v_cvt_pk_bf16_f32 v71, v86, v90
	v_lshl_add_u64 v[72:73], v[72:73], 1, v[88:89]
	v_add_u32_e32 v2, s35, v109
	global_store_dwordx4 v[72:73], v[68:71], off nt
	v_mad_u64_u32 v[72:73], s[0:1], v2, s25, 0
	v_ashrrev_i32_e32 v74, 31, v2
	v_mov_b32_e32 v2, v73
	v_cvt_pk_bf16_f32 v68, v75, v77
	v_mad_u64_u32 v[74:75], s[0:1], v74, s25, v[2:3]
	v_mov_b32_e32 v73, v74
	v_cvt_pk_bf16_f32 v69, v79, v81
	v_cvt_pk_bf16_f32 v70, v83, v85
	v_cvt_pk_bf16_f32 v71, v87, v91
	v_lshl_add_u64 v[72:73], v[72:73], 1, v[88:89]
	global_store_dwordx4 v[72:73], v[68:71], off nt
	s_waitcnt lgkmcnt(0)
	v_mov_b32_e32 v72, v36
	v_mov_b32_e32 v73, v37
	v_mov_b32_e32 v68, v40
	v_mov_b32_e32 v69, v41
	v_mov_b32_e32 v70, v42
	v_mov_b32_e32 v71, v43
	v_mov_b32_e32 v74, v38
	v_mov_b32_e32 v75, v39
	v_mov_b32_e32 v76, v48
	v_mov_b32_e32 v77, v49
	v_mov_b32_e32 v78, v50
	v_mov_b32_e32 v79, v51
	v_mov_b32_e32 v80, v44
	v_mov_b32_e32 v81, v45
	v_mov_b32_e32 v82, v46
	v_mov_b32_e32 v83, v47
	v_mov_b32_e32 v84, v60
	v_mov_b32_e32 v85, v61
	v_mov_b32_e32 v86, v62
	v_mov_b32_e32 v87, v63
	v_mov_b32_e32 v88, v52
	v_mov_b32_e32 v89, v53
	v_mov_b32_e32 v90, v54
	v_mov_b32_e32 v91, v55
	v_mov_b32_e32 v92, v64
	v_mov_b32_e32 v93, v65
	v_mov_b32_e32 v94, v66
	v_mov_b32_e32 v95, v67
	v_mov_b32_e32 v96, v56
	v_mov_b32_e32 v97, v57
	v_mov_b32_e32 v98, v58
	s_cmp_ge_i32 s31, s26
	v_mov_b32_e32 v99, v59
	s_cbranch_scc1 .LBB0_1644
	v_mov_b64_e32 v[58:59], v[30:31]
	v_mov_b64_e32 v[66:67], v[34:35]
	v_mov_b64_e32 v[54:55], v[22:23]
	v_mov_b64_e32 v[62:63], v[26:27]
	v_mov_b64_e32 v[46:47], v[14:15]
	v_mov_b64_e32 v[50:51], v[18:19]
	v_mov_b64_e32 v[38:39], v[6:7]
	v_mov_b64_e32 v[42:43], v[10:11]
	v_mov_b64_e32 v[56:57], v[28:29]
	v_mov_b64_e32 v[64:65], v[32:33]
	v_mov_b64_e32 v[52:53], v[20:21]
	v_mov_b64_e32 v[60:61], v[24:25]
	v_mov_b64_e32 v[44:45], v[12:13]
	v_mov_b64_e32 v[48:49], v[16:17]
	v_mov_b64_e32 v[36:37], v[4:5]
	v_mov_b64_e32 v[40:41], v[8:9]
	s_mov_b32 s35, s12
	s_mov_b32 s8, s11
	s_branch .LBB0_1692
